# speedup vs baseline: 1.0328x; 1.0042x over previous
_Z11prep_kernelPKfS0_S0_S0_S0_PKiPDF16_S3_S3_PyPi:
	s_cmpk_gt_i32 s2, 0x7ff
	s_mov_b64 s[4:5], -1
	s_cbranch_scc0 .LBB0_22
	s_cmpk_gt_u32 s2, 0xbff
	v_lshrrev_b32_e32 v1, 6, v0
	v_and_b32_e32 v2, 63, v0
	s_cbranch_scc0 .LBB0_11
	s_load_dwordx2 s[4:5], s[0:1], 0x28
	s_add_i32 s40, s2, 0xfffff400
	s_lshl_b32 s6, s40, 1
	s_and_b32 s33, s6, 0x7fffffc0
	v_lshlrev_b32_e32 v3, 4, v1
	v_or_b32_e32 v4, s33, v3
	v_mov_b32_e32 v5, 0
	s_and_b32 s3, s2, 31
	v_lshlrev_b64 v[6:7], 13, v[4:5]
	s_mov_b32 s43, 0
	s_waitcnt lgkmcnt(0)
	v_lshl_add_u64 v[6:7], s[4:5], 0, v[6:7]
	s_lshl_b32 s42, s3, 8
	v_lshl_add_u64 v[6:7], v[6:7], 0, s[42:43]
	v_lshlrev_b32_e32 v4, 2, v2
	v_lshl_add_u64 v[6:7], v[6:7], 0, v[4:5]
	s_movk_i32 s4, 0x2000
	v_add_co_u32_e32 v8, vcc, s4, v6
	s_movk_i32 s4, 0x4000
	s_nop 0
	v_addc_co_u32_e32 v9, vcc, 0, v7, vcc
	v_add_co_u32_e32 v10, vcc, s4, v6
	s_movk_i32 s4, 0x6000
	s_nop 0
	v_addc_co_u32_e32 v11, vcc, 0, v7, vcc
	v_add_co_u32_e32 v12, vcc, s4, v6
	s_mov_b32 s4, 0x8000
	s_nop 0
	v_addc_co_u32_e32 v13, vcc, 0, v7, vcc
	v_add_co_u32_e32 v14, vcc, s4, v6
	s_mov_b32 s4, 0xa000
	s_nop 0
	v_addc_co_u32_e32 v15, vcc, 0, v7, vcc
	v_add_co_u32_e32 v16, vcc, s4, v6
	s_mov_b32 s4, 0xc000
	s_nop 0
	v_addc_co_u32_e32 v17, vcc, 0, v7, vcc
	v_add_co_u32_e32 v18, vcc, s4, v6
	s_mov_b32 s4, 0xe000
	s_nop 0
	v_addc_co_u32_e32 v19, vcc, 0, v7, vcc
	v_add_co_u32_e32 v20, vcc, s4, v6
	s_mov_b32 s4, 0x10000
	s_nop 0
	v_addc_co_u32_e32 v21, vcc, 0, v7, vcc
	global_load_dword v4, v[6:7], off nt
	global_load_dword v22, v[8:9], off nt
	global_load_dword v23, v[10:11], off nt
	global_load_dword v24, v[12:13], off nt
	global_load_dword v25, v[14:15], off nt
	global_load_dword v26, v[16:17], off nt
	global_load_dword v27, v[18:19], off nt
	global_load_dword v28, v[20:21], off nt
	v_add_co_u32_e32 v8, vcc, s4, v6
	s_mov_b32 s4, 0x12000
	s_nop 0
	v_addc_co_u32_e32 v9, vcc, 0, v7, vcc
	v_add_co_u32_e32 v10, vcc, s4, v6
	s_mov_b32 s4, 0x14000
	s_nop 0
	v_addc_co_u32_e32 v11, vcc, 0, v7, vcc
	v_add_co_u32_e32 v12, vcc, s4, v6
	s_mov_b32 s4, 0x16000
	s_nop 0
	v_addc_co_u32_e32 v13, vcc, 0, v7, vcc
	v_add_co_u32_e32 v14, vcc, s4, v6
	s_mov_b32 s4, 0x18000
	s_nop 0
	v_addc_co_u32_e32 v15, vcc, 0, v7, vcc
	v_add_co_u32_e32 v16, vcc, s4, v6
	s_mov_b32 s4, 0x1a000
	s_nop 0
	v_addc_co_u32_e32 v17, vcc, 0, v7, vcc
	v_add_co_u32_e32 v18, vcc, s4, v6
	s_mov_b32 s4, 0x1c000
	s_nop 0
	v_addc_co_u32_e32 v19, vcc, 0, v7, vcc
	v_add_co_u32_e32 v20, vcc, s4, v6
	s_mov_b32 s4, 0x1e000
	s_nop 0
	v_addc_co_u32_e32 v21, vcc, 0, v7, vcc
	v_add_co_u32_e32 v6, vcc, s4, v6
	v_cmp_eq_u32_e64 s[36:37], 0, v2
	s_nop 0
	v_addc_co_u32_e32 v7, vcc, 0, v7, vcc
	global_load_dword v29, v[8:9], off nt
	global_load_dword v30, v[10:11], off nt
	global_load_dword v31, v[12:13], off nt
	global_load_dword v32, v[14:15], off nt
	global_load_dword v33, v[16:17], off nt
	global_load_dword v34, v[18:19], off nt
	global_load_dword v35, v[20:21], off nt
	global_load_dword v36, v[6:7], off nt
	v_cmp_gt_u32_e64 s[38:39], 16, v2
	s_waitcnt vmcnt(15)
	v_cmp_ne_u32_e64 s[26:27], 0, v4
	s_waitcnt vmcnt(14)
	v_cmp_ne_u32_e64 s[34:35], 0, v22
	s_waitcnt vmcnt(13)
	v_cmp_ne_u32_e64 s[30:31], 0, v23
	s_waitcnt vmcnt(12)
	v_cmp_ne_u32_e64 s[28:29], 0, v24
	s_waitcnt vmcnt(11)
	v_cmp_ne_u32_e64 s[24:25], 0, v25
	s_waitcnt vmcnt(10)
	v_cmp_ne_u32_e64 s[22:23], 0, v26
	s_waitcnt vmcnt(9)
	v_cmp_ne_u32_e64 s[20:21], 0, v27
	s_waitcnt vmcnt(8)
	v_cmp_ne_u32_e64 s[18:19], 0, v28
	s_waitcnt vmcnt(7)
	v_cmp_ne_u32_e64 s[16:17], 0, v29
	s_waitcnt vmcnt(6)
	v_cmp_ne_u32_e64 s[14:15], 0, v30
	s_waitcnt vmcnt(5)
	v_cmp_ne_u32_e64 s[12:13], 0, v31
	s_waitcnt vmcnt(4)
	v_cmp_ne_u32_e64 s[10:11], 0, v32
	s_waitcnt vmcnt(3)
	v_cmp_ne_u32_e64 s[8:9], 0, v33
	s_waitcnt vmcnt(2)
	v_cmp_ne_u32_e64 s[6:7], 0, v34
	s_waitcnt vmcnt(1)
	v_cmp_ne_u32_e64 s[4:5], 0, v35
	s_waitcnt vmcnt(0)
	v_cmp_ne_u32_e32 vcc, 0, v36
	s_and_saveexec_b64 s[44:45], s[38:39]
	s_cbranch_execz .LBB0_4
	v_mov_b32_e32 v6, s27
	v_mov_b32_e32 v4, s26
	v_cndmask_b32_e64 v6, 0, v6, s[36:37]
	v_mov_b32_e32 v7, s35
	v_cmp_eq_u32_e64 s[38:39], 1, v2
	v_cndmask_b32_e64 v4, 0, v4, s[36:37]
	s_load_dwordx2 s[46:47], s[0:1], 0x48
	v_cndmask_b32_e64 v6, v6, v7, s[38:39]
	v_mov_b32_e32 v7, s34
	v_cndmask_b32_e64 v4, v4, v7, s[38:39]
	v_mov_b32_e32 v7, s30
	v_cmp_eq_u32_e64 s[38:39], 2, v2
	s_lshl_b32 s3, s3, 11
	s_add_i32 s42, s33, s3
	v_cndmask_b32_e64 v4, v4, v7, s[38:39]
	v_mov_b32_e32 v7, s31
	v_cndmask_b32_e64 v6, v6, v7, s[38:39]
	v_mov_b32_e32 v7, s29
	v_cmp_eq_u32_e64 s[38:39], 3, v2
	s_nop 1
	v_cndmask_b32_e64 v6, v6, v7, s[38:39]
	v_mov_b32_e32 v7, s28
	v_cndmask_b32_e64 v4, v4, v7, s[38:39]
	v_mov_b32_e32 v7, s24
	v_cmp_eq_u32_e64 s[38:39], 4, v2
	s_nop 1
	v_cndmask_b32_e64 v4, v4, v7, s[38:39]
	v_mov_b32_e32 v7, s25
	v_cndmask_b32_e64 v6, v6, v7, s[38:39]
	v_mov_b32_e32 v7, s23
	v_cmp_eq_u32_e64 s[38:39], 5, v2
	s_nop 1
	v_cndmask_b32_e64 v6, v6, v7, s[38:39]
	v_mov_b32_e32 v7, s22
	v_cndmask_b32_e64 v4, v4, v7, s[38:39]
	v_mov_b32_e32 v7, s20
	v_cmp_eq_u32_e64 s[38:39], 6, v2
	s_nop 1
	v_cndmask_b32_e64 v4, v4, v7, s[38:39]
	v_mov_b32_e32 v7, s21
	v_cndmask_b32_e64 v6, v6, v7, s[38:39]
	v_mov_b32_e32 v7, s19
	v_cmp_eq_u32_e64 s[38:39], 7, v2
	s_nop 1
	v_cndmask_b32_e64 v6, v6, v7, s[38:39]
	v_mov_b32_e32 v7, s18
	v_cndmask_b32_e64 v4, v4, v7, s[38:39]
	v_mov_b32_e32 v7, s16
	v_cmp_eq_u32_e64 s[38:39], 8, v2
	s_nop 1
	v_cndmask_b32_e64 v4, v4, v7, s[38:39]
	v_mov_b32_e32 v7, s17
	v_cndmask_b32_e64 v6, v6, v7, s[38:39]
	v_mov_b32_e32 v7, s15
	v_cmp_eq_u32_e64 s[38:39], 9, v2
	s_nop 1
	v_cndmask_b32_e64 v6, v6, v7, s[38:39]
	v_mov_b32_e32 v7, s14
	v_cndmask_b32_e64 v4, v4, v7, s[38:39]
	v_mov_b32_e32 v7, s12
	v_cmp_eq_u32_e64 s[38:39], 10, v2
	s_nop 1
	v_cndmask_b32_e64 v4, v4, v7, s[38:39]
	v_mov_b32_e32 v7, s13
	v_cndmask_b32_e64 v6, v6, v7, s[38:39]
	v_mov_b32_e32 v7, s11
	v_cmp_eq_u32_e64 s[38:39], 11, v2
	s_nop 1
	v_cndmask_b32_e64 v6, v6, v7, s[38:39]
	v_mov_b32_e32 v7, s10
	v_cndmask_b32_e64 v4, v4, v7, s[38:39]
	v_mov_b32_e32 v7, s8
	v_cmp_eq_u32_e64 s[38:39], 12, v2
	s_nop 1
	v_cndmask_b32_e64 v4, v4, v7, s[38:39]
	v_mov_b32_e32 v7, s9
	v_cndmask_b32_e64 v6, v6, v7, s[38:39]
	v_mov_b32_e32 v7, s7
	v_cmp_eq_u32_e64 s[38:39], 13, v2
	s_nop 1
	v_cndmask_b32_e64 v6, v6, v7, s[38:39]
	v_mov_b32_e32 v7, s6
	v_cndmask_b32_e64 v4, v4, v7, s[38:39]
	v_mov_b32_e32 v7, s4
	v_cmp_eq_u32_e64 s[38:39], 14, v2
	s_nop 1
	v_cndmask_b32_e64 v4, v4, v7, s[38:39]
	v_mov_b32_e32 v7, s5
	v_cndmask_b32_e64 v6, v6, v7, s[38:39]
	v_mov_b32_e32 v7, vcc_hi
	v_cmp_eq_u32_e64 s[38:39], 15, v2
	s_nop 1
	v_cndmask_b32_e64 v7, v6, v7, s[38:39]
	v_mov_b32_e32 v6, vcc_lo
	v_cndmask_b32_e64 v6, v4, v6, s[38:39]
	s_lshl_b64 s[38:39], s[42:43], 3
	s_waitcnt lgkmcnt(0)
	s_add_u32 s38, s46, s38
	s_addc_u32 s39, s47, s39
	v_lshlrev_b32_e32 v4, 3, v3
	v_lshl_add_u64 v[8:9], s[38:39], 0, v[4:5]
	v_lshlrev_b32_e32 v4, 3, v2
	v_lshl_add_u64 v[4:5], v[8:9], 0, v[4:5]
	global_store_dwordx2 v[4:5], v[6:7], off sc1

.LBB0_9:
	s_mov_b32 s41, 0
	s_lshl_b64 s[8:9], s[40:41], 2
	s_add_u32 s6, s6, s8
	s_addc_u32 s7, s7, s9
	global_store_dword v3, v4, s[6:7] sc1
